# speedup vs baseline: 1.0023x; 1.0023x over previous
.LBB3_11:
	v_pk_mul_f32 v[4:5], v[98:99], v[34:35]
	s_xor_b64 s[2:3], s[0:1], -1
	v_exp_f32_e32 v6, v5
	v_exp_f32_e32 v7, v4
	v_pk_mul_f32 v[4:5], v[34:35], v[18:19]
	s_nop 0
	v_fma_f32 v5, v48, v6, v5
	v_fmac_f32_e32 v4, v7, v5
	v_pk_fma_f32 v[10:11], v[2:3], v[4:5], v[100:101]
	s_cmp_lg_u32 s6, 0
	s_cbranch_scc1 .Lp3_nobar
	s_waitcnt lgkmcnt(0)
	s_barrier
	v_lshl_add_u32 v6, v137, 1, v135
	ds_read_b128 v[2:5], v6
	ds_read_b128 v[6:9], v6 offset:16
	s_cmpk_gt_i32 s66, 0x2ff
	s_cbranch_scc1 .Lp3_epi
	s_add_i32 s43, s66, 0x300
	s_ashr_i32 s60, s43, 3
	s_mul_hi_i32 s61, s60, 0x55555556
	s_lshr_b32 s62, s61, 31
	s_add_i32 s61, s61, s62
	s_mul_i32 s62, s61, 0x3fffffd
	s_add_i32 s62, s62, s60
	s_lshl_b32 s62, s62, 6
	s_lshl_b32 s63, s43, 5
	s_and_b32 s63, s63, 32
	s_or_b32 s62, s62, s63
	s_bfe_u32 s63, s43, 0x20001
	s_mul_i32 s63, s63, 0xc0
	s_add_i32 s62, s62, s63
	s_lshl_b32 s62, s62, 7
	s_lshl_b32 s63, s61, 1
	s_and_b32 s63, s63, -16
	s_add_i32 s62, s62, s63
	s_lshl_b32 s62, s62, 9
	s_lshl_b32 s63, s61, 4
	s_and_b32 s63, s63, 0x70
	s_lshl_b32 s63, s63, 2
	s_add_i32 s62, s62, s63
	s_add_u32 s44, s64, s62
	s_addc_u32 s45, s65, 0
	s_add_u32 s46, s44, 0x40000
	s_addc_u32 s47, s45, 0
	s_add_u32 s48, s46, 0x40000
	s_addc_u32 s49, s47, 0
	s_add_u32 s50, s48, 0x40000
	s_addc_u32 s51, s49, 0
	s_add_u32 s52, s50, 0x40000
	s_addc_u32 s53, s51, 0
	s_add_u32 s54, s52, 0x40000
	s_addc_u32 s55, s53, 0
	s_add_u32 s56, s54, 0x40000
	s_addc_u32 s57, s55, 0
	s_add_u32 s58, s56, 0x40000
	s_addc_u32 s59, s57, 0
	global_load_dwordx4 v[164:167], v162, s[44:45]
	global_load_dwordx4 v[164:167], v162, s[46:47]
	global_load_dwordx4 v[164:167], v162, s[48:49]
	global_load_dwordx4 v[164:167], v162, s[50:51]
	global_load_dwordx4 v[164:167], v162, s[52:53]
	global_load_dwordx4 v[164:167], v162, s[54:55]
	global_load_dwordx4 v[164:167], v162, s[56:57]
	global_load_dwordx4 v[164:167], v162, s[58:59]
	s_branch .Lp3_epi

.Lp3_epi:
	v_pk_fma_f32 v[10:11], v[94:95], v[86:87], v[10:11]
	v_pk_fma_f32 v[12:13], v[94:95], v[88:89], v[128:129]
	v_pk_fma_f32 v[14:15], v[94:95], v[82:83], v[36:37]
	s_waitcnt lgkmcnt(1)
	v_fma_mix_f32 v10, v2, 1.0, v10 op_sel_hi:[1,0,0]
	v_fma_mix_f32 v11, v2, 1.0, v11 op_sel:[1,0,0] op_sel_hi:[1,0,0]
	v_fma_mix_f32 v12, v3, 1.0, v12 op_sel_hi:[1,0,0]
	v_fma_mix_f32 v13, v3, 1.0, v13 op_sel:[1,0,0] op_sel_hi:[1,0,0]
	ds_write_b128 v136, v[10:13]
	v_fma_mix_f32 v2, v4, 1.0, v14 op_sel_hi:[1,0,0]
	v_fma_mix_f32 v3, v4, 1.0, v15 op_sel:[1,0,0] op_sel_hi:[1,0,0]
	v_pk_fma_f32 v[10:11], v[94:95], v[84:85], v[38:39]
	v_fma_mix_f32 v4, v5, 1.0, v10 op_sel_hi:[1,0,0]
	v_fma_mix_f32 v5, v5, 1.0, v11 op_sel:[1,0,0] op_sel_hi:[1,0,0]
	ds_write_b128 v136, v[2:5] offset:16
	v_pk_fma_f32 v[10:11], v[94:95], v[78:79], v[40:41]
	v_pk_fma_f32 v[12:13], v[94:95], v[80:81], v[42:43]
	v_pk_fma_f32 v[2:3], v[94:95], v[74:75], v[44:45]
	v_pk_fma_f32 v[4:5], v[94:95], v[76:77], v[46:47]
	s_waitcnt lgkmcnt(2)
	v_fma_mix_f32 v10, v6, 1.0, v10 op_sel_hi:[1,0,0]
	v_fma_mix_f32 v11, v6, 1.0, v11 op_sel:[1,0,0] op_sel_hi:[1,0,0]
	v_fma_mix_f32 v12, v7, 1.0, v12 op_sel_hi:[1,0,0]
	v_fma_mix_f32 v13, v7, 1.0, v13 op_sel:[1,0,0] op_sel_hi:[1,0,0]
	ds_write_b128 v136, v[10:13] offset:32
	v_fma_mix_f32 v2, v8, 1.0, v2 op_sel_hi:[1,0,0]
	v_fma_mix_f32 v3, v8, 1.0, v3 op_sel:[1,0,0] op_sel_hi:[1,0,0]
	v_fma_mix_f32 v4, v9, 1.0, v4 op_sel_hi:[1,0,0]
	v_fma_mix_f32 v5, v9, 1.0, v5 op_sel:[1,0,0] op_sel_hi:[1,0,0]
	ds_write_b128 v136, v[2:5] offset:48
	v_mov_b64_e32 v[92:93], v[64:65]
	v_mov_b64_e32 v[18:19], v[58:59]
	s_movk_i32 s6, 0x80
	s_mov_b64 s[0:1], 0
	s_andn2_b64 vcc, exec, s[2:3]
	v_mov_b32_e32 v138, v133
	v_mov_b32_e32 v139, v132
	v_mov_b64_e32 v[90:91], v[62:63]
	v_mov_b64_e32 v[20:21], v[60:61]
	s_cbranch_vccz .LBB3_19
